# baseline (speedup 1.0000x reference)
.LBB1_8:
	s_lshl_b32 s12, s62, 9
	v_lshl_add_u64 v[6:7], s[12:13], 4, v[210:211]
	v_add_co_u32_e32 v34, vcc, s52, v6
	s_mov_b32 s12, s13
	s_nop 0
	v_addc_co_u32_e32 v35, vcc, 0, v7, vcc
	global_load_dwordx4 v[2:5], v[34:35], off offset:-4096
	v_add_co_u32_e32 v36, vcc, s49, v6
	s_xor_b64 s[50:51], s[14:15], -1
	s_nop 0
	v_addc_co_u32_e32 v37, vcc, 0, v7, vcc
	global_load_dwordx4 v[6:9], v[36:37], off offset:1024
	global_load_dwordx4 v[10:13], v[36:37], off offset:2048
	global_load_dwordx4 v[14:17], v[34:35], off
	s_mov_b32 s14, s13
	s_mov_b32 s15, s13
	s_mov_b32 s16, s13
	s_mov_b32 s17, s13
	s_mov_b32 s18, s13
	s_mov_b32 s19, s13
	s_mov_b32 s20, s13
	s_mov_b32 s21, s13
	s_mov_b32 s22, s13
	s_mov_b32 s23, s13
	s_mov_b32 s24, s13
	s_mov_b32 s25, s13
	s_mov_b32 s26, s13
	s_mov_b32 s27, s13
	s_waitcnt vmcnt(3) lgkmcnt(7)
	v_mfma_f32_32x32x16_f16 v[18:33], v[2:5], v[146:149], 0
	global_load_dwordx4 v[2:5], v[36:37], off offset:3072
	s_waitcnt vmcnt(3) lgkmcnt(6)
	v_mfma_f32_32x32x16_f16 v[18:33], v[6:9], v[150:153], v[18:33]
	global_load_dwordx4 v[6:9], v[34:35], off offset:1024
	s_waitcnt vmcnt(3) lgkmcnt(5)
	v_mfma_f32_32x32x16_f16 v[18:33], v[10:13], v[154:157], v[18:33]
	global_load_dwordx4 v[10:13], v[34:35], off offset:2048
	s_nop 0
	global_load_dwordx4 v[34:37], v[34:35], off offset:3072
	s_waitcnt vmcnt(3) lgkmcnt(4)
	v_mfma_f32_32x32x16_f16 v[18:33], v[2:5], v[158:161], v[18:33]
	s_waitcnt lgkmcnt(3)
	v_mfma_f32_32x32x16_f16 v[18:33], v[14:17], v[162:165], v[18:33]
	s_waitcnt vmcnt(2) lgkmcnt(2)
	v_mfma_f32_32x32x16_f16 v[18:33], v[6:9], v[166:169], v[18:33]
	s_waitcnt vmcnt(1) lgkmcnt(1)
	v_mfma_f32_32x32x16_f16 v[18:33], v[10:13], v[170:173], v[18:33]
	v_mov_b64_e32 v[2:3], s[12:13]
	v_mov_b64_e32 v[4:5], s[14:15]
	v_mov_b64_e32 v[6:7], s[16:17]
	v_mov_b64_e32 v[8:9], s[18:19]
	v_mov_b64_e32 v[10:11], s[20:21]
	v_mov_b64_e32 v[12:13], s[22:23]
	v_mov_b64_e32 v[14:15], s[24:25]
	s_waitcnt vmcnt(0) lgkmcnt(0)
	v_mfma_f32_32x32x16_f16 v[18:33], v[34:37], v[174:177], v[18:33]
	v_mov_b64_e32 v[16:17], s[26:27]
	s_mul_i32 s12, s62, 20
	s_lshl_b64 s[14:15], s[12:13], 2
	s_add_u32 s14, s10, s14
	s_addc_u32 s15, s11, s15
	s_load_dwordx16 s[16:31], s[14:15], 0x0
	s_load_dwordx4 s[40:43], s[14:15], 0x40
	s_mul_i32 s12, s62, 0x1b0000
	s_nop 3
	ds_bpermute_b32 v34, v225, v18
	ds_bpermute_b32 v35, v225, v19
	ds_bpermute_b32 v36, v225, v20
	ds_bpermute_b32 v37, v225, v21
	ds_bpermute_b32 v38, v225, v22
	ds_bpermute_b32 v39, v225, v23
	ds_bpermute_b32 v40, v225, v24
	ds_bpermute_b32 v41, v225, v25
	ds_bpermute_b32 v42, v225, v26
	ds_bpermute_b32 v43, v225, v27
	ds_bpermute_b32 v44, v225, v28
	ds_bpermute_b32 v45, v225, v29
	ds_bpermute_b32 v46, v225, v30
	ds_bpermute_b32 v47, v225, v31
	ds_bpermute_b32 v48, v225, v32
	ds_bpermute_b32 v49, v225, v33
	s_waitcnt lgkmcnt(0)
	v_cndmask_b32_e64 v50, v34, v18, s[0:1]
	v_cndmask_b32_e64 v19, v35, v19, s[0:1]
	v_cndmask_b32_e64 v20, v36, v20, s[0:1]
	v_cndmask_b32_e64 v21, v37, v21, s[0:1]
	v_cndmask_b32_e64 v18, v18, v34, s[0:1]
	v_cndmask_b32_e64 v34, v38, v22, s[0:1]
	v_cndmask_b32_e64 v23, v39, v23, s[0:1]
	v_cndmask_b32_e64 v24, v40, v24, s[0:1]
	v_cndmask_b32_e64 v25, v41, v25, s[0:1]
	v_cndmask_b32_e64 v22, v22, v38, s[0:1]
	v_add_f32_e32 v37, s16, v50
	v_add_f32_e32 v19, s17, v19
	v_add_f32_e32 v20, s18, v20
	v_add_f32_e32 v21, s19, v21
	v_add_f32_e32 v34, s21, v34
	v_add_f32_e32 v23, s22, v23
	v_add_f32_e32 v24, s23, v24
	v_add_f32_e32 v25, s24, v25
	v_cndmask_b32_e64 v35, v42, v26, s[0:1]
	v_cndmask_b32_e64 v27, v43, v27, s[0:1]
	v_cndmask_b32_e64 v28, v44, v28, s[0:1]
	v_cndmask_b32_e64 v29, v45, v29, s[0:1]
	v_add_f32_e32 v18, s20, v18
	v_add_f32_e32 v22, s25, v22
	v_max_f32_e32 v38, v37, v19
	v_max_f32_e32 v39, v20, v21
	v_max_f32_e32 v40, v34, v23
	v_max_f32_e32 v41, v24, v25
	v_cndmask_b32_e64 v26, v26, v42, s[0:1]
	v_cndmask_b32_e64 v36, v46, v30, s[0:1]
	v_cndmask_b32_e64 v31, v47, v31, s[0:1]
	v_cndmask_b32_e64 v32, v48, v32, s[0:1]
	v_add_f32_e32 v35, s26, v35
	v_add_f32_e32 v27, s27, v27
	v_add_f32_e32 v28, s28, v28
	v_add_f32_e32 v29, s29, v29
	v_max3_f32 v38, v38, v39, v18
	v_max3_f32 v39, v40, v41, v22
	v_cndmask_b32_e64 v33, v49, v33, s[0:1]
	v_add_f32_e32 v26, s30, v26
	v_add_f32_e32 v36, s31, v36
	v_add_f32_e32 v31, s40, v31
	v_add_f32_e32 v32, s41, v32
	v_max_f32_e32 v42, v35, v27
	v_max_f32_e32 v43, v28, v29
	v_sub_f32_e32 v34, v34, v39
	v_add_f32_e32 v33, s42, v33
	v_cndmask_b32_e64 v30, v30, v46, s[0:1]
	v_max3_f32 v40, v42, v43, v26
	v_sub_f32_e32 v37, v37, v38
	v_sub_f32_e32 v23, v23, v39
	v_mul_f32_e32 v34, 0x3fb8aa3b, v34
	v_add_f32_e32 v30, s43, v30
	v_max_f32_e32 v41, v36, v31
	v_max_f32_e32 v42, v32, v33
	v_sub_f32_e32 v19, v19, v38
	v_sub_f32_e32 v24, v24, v39
	v_sub_f32_e32 v35, v35, v40
	v_mul_f32_e32 v37, 0x3fb8aa3b, v37
	v_mul_f32_e32 v23, 0x3fb8aa3b, v23
	v_exp_f32_e32 v34, v34
	v_max3_f32 v41, v41, v42, v30
	v_sub_f32_e32 v20, v20, v38
	v_sub_f32_e32 v25, v25, v39
	v_sub_f32_e32 v27, v27, v40
	v_mul_f32_e32 v19, 0x3fb8aa3b, v19
	v_mul_f32_e32 v24, 0x3fb8aa3b, v24
	v_mul_f32_e32 v35, 0x3fb8aa3b, v35
	v_exp_f32_e32 v37, v37
	v_exp_f32_e32 v23, v23
	v_sub_f32_e32 v36, v36, v41
	v_sub_f32_e32 v21, v21, v38
	v_sub_f32_e32 v22, v22, v39
	v_sub_f32_e32 v28, v28, v40
	v_mul_f32_e32 v20, 0x3fb8aa3b, v20
	v_mul_f32_e32 v25, 0x3fb8aa3b, v25
	v_mul_f32_e32 v27, 0x3fb8aa3b, v27
	v_exp_f32_e32 v19, v19
	v_exp_f32_e32 v24, v24
	v_exp_f32_e32 v35, v35
	v_mul_f32_e32 v36, 0x3fb8aa3b, v36
	v_sub_f32_e32 v31, v31, v41
	v_sub_f32_e32 v18, v18, v38
	v_sub_f32_e32 v29, v29, v40
	v_mul_f32_e32 v21, 0x3fb8aa3b, v21
	v_mul_f32_e32 v22, 0x3fb8aa3b, v22
	v_mul_f32_e32 v28, 0x3fb8aa3b, v28
	v_exp_f32_e32 v20, v20
	v_exp_f32_e32 v25, v25
	v_exp_f32_e32 v27, v27
	v_exp_f32_e32 v36, v36
	v_mul_f32_e32 v31, 0x3fb8aa3b, v31
	v_sub_f32_e32 v32, v32, v41
	v_sub_f32_e32 v26, v26, v40
	v_mul_f32_e32 v18, 0x3fb8aa3b, v18
	v_mul_f32_e32 v29, 0x3fb8aa3b, v29
	v_exp_f32_e32 v21, v21
	v_exp_f32_e32 v22, v22
	v_exp_f32_e32 v28, v28
	v_add_f32_e32 v39, 0, v34
	v_exp_f32_e32 v31, v31
	v_mul_f32_e32 v32, 0x3fb8aa3b, v32
	v_sub_f32_e32 v33, v33, v41
	v_mul_f32_e32 v26, 0x3fb8aa3b, v26
	v_exp_f32_e32 v18, v18
	v_exp_f32_e32 v29, v29
	v_add_f32_e32 v38, 0, v37
	v_add_f32_e32 v39, v23, v39
	v_exp_f32_e32 v32, v32
	v_mul_f32_e32 v33, 0x3fb8aa3b, v33
	v_sub_f32_e32 v30, v30, v41
	v_exp_f32_e32 v26, v26
	v_add_f32_e32 v40, 0, v35
	v_add_f32_e32 v38, v19, v38
	v_add_f32_e32 v39, v24, v39
	v_exp_f32_e32 v33, v33
	v_mul_f32_e32 v30, 0x3fb8aa3b, v30
	v_add_f32_e32 v40, v27, v40
	v_add_f32_e32 v38, v20, v38
	v_add_f32_e32 v39, v25, v39
	v_add_f32_e32 v42, 0, v36
	v_exp_f32_e32 v30, v30
	v_add_f32_e32 v38, v21, v38
	v_add_f32_e32 v39, v22, v39
	v_add_f32_e32 v40, v28, v40
	v_add_f32_e32 v41, v31, v42
	v_add_f32_e32 v38, v18, v38
	v_rcp_f32_e32 v39, v39
	v_add_f32_e32 v40, v29, v40
	v_add_f32_e32 v41, v32, v41
	v_rcp_f32_e32 v38, v38
	v_add_f32_e32 v40, v26, v40
	v_add_f32_e32 v41, v33, v41
	v_rcp_f32_e32 v40, v40
	v_add_f32_e32 v41, v30, v41
	v_rcp_f32_e32 v41, v41
	v_mul_f32_e32 v34, v34, v39
	v_mul_f32_e32 v23, v23, v39
	v_fmac_f32_e32 v34, v37, v38
	v_fmac_f32_e32 v23, v19, v38
	v_mul_f32_e32 v24, v24, v39
	v_fmac_f32_e32 v34, v35, v40
	v_fmac_f32_e32 v23, v27, v40
	v_mul_f32_e32 v22, v22, v39
	v_mul_f32_e32 v29, v29, v40
	v_fmac_f32_e32 v34, v36, v41
	v_fmac_f32_e32 v23, v31, v41
	v_fmac_f32_e32 v24, v20, v38
	v_fmac_f32_e32 v24, v28, v40
	v_cndmask_b32_e64 v20, v22, v34, s[4:5]
	v_cndmask_b32_e64 v22, v29, v23, s[4:5]
	v_mul_f32_e32 v21, v21, v38
	v_mul_f32_e32 v18, v18, v38
	v_mul_f32_e32 v25, v25, v39
	v_mul_f32_e32 v26, v26, v40
	v_mul_f32_e32 v33, v33, v41
	v_mul_f32_e32 v30, v30, v41
	v_fmac_f32_e32 v24, v32, v41
	v_mul_f32_e32 v20, 0x3e800000, v20
	v_mul_f32_e32 v22, 0x3e800000, v22
	v_mul_f32_e32 v19, 0x3e800000, v25
	ds_write2st64_b32 v222, v20, v22 offset1:8
	v_cndmask_b32_e64 v20, v26, v24, s[4:5]
	v_cndmask_b32_e64 v21, v33, v21, s[4:5]
	v_cndmask_b32_e64 v18, v30, v18, s[4:5]
	v_mul_f32_e32 v20, 0x3e800000, v20
	v_mul_f32_e32 v21, 0x3e800000, v21
	v_mul_f32_e32 v18, 0x3e800000, v18
	v_cndmask_b32_e64 v19, 0, v19, s[4:5]
	ds_write2st64_b32 v222, v20, v21 offset0:16 offset1:24
	ds_write2st64_b32 v222, v18, v19 offset0:32 offset1:40
	s_mul_hi_u32 s14, s62, 0x1b0000
	s_add_u32 s12, s44, s12
	v_mov_b64_e32 v[64:65], v[16:17]
	v_mov_b64_e32 v[48:49], v[16:17]
	v_mov_b64_e32 v[32:33], v[16:17]
	s_addc_u32 s16, s45, s14
	s_mov_b32 s17, 0
	v_mov_b64_e32 v[62:63], v[14:15]
	v_mov_b64_e32 v[60:61], v[12:13]
	v_mov_b64_e32 v[58:59], v[10:11]
	v_mov_b64_e32 v[56:57], v[8:9]
	v_mov_b64_e32 v[54:55], v[6:7]
	v_mov_b64_e32 v[52:53], v[4:5]
	v_mov_b64_e32 v[50:51], v[2:3]
	v_mov_b64_e32 v[46:47], v[14:15]
	v_mov_b64_e32 v[44:45], v[12:13]
	v_mov_b64_e32 v[42:43], v[10:11]
	v_mov_b64_e32 v[40:41], v[8:9]
	v_mov_b64_e32 v[38:39], v[6:7]
	v_mov_b64_e32 v[36:37], v[4:5]
	v_mov_b64_e32 v[34:35], v[2:3]
	v_mov_b64_e32 v[30:31], v[14:15]
	v_mov_b64_e32 v[28:29], v[12:13]
	v_mov_b64_e32 v[26:27], v[10:11]
	v_mov_b64_e32 v[24:25], v[8:9]
	v_mov_b64_e32 v[22:23], v[6:7]
	v_mov_b64_e32 v[20:21], v[4:5]
	v_mov_b64_e32 v[18:19], v[2:3]
	s_mov_b32 s18, 0
	v_readfirstlane_b32 s28, v0
	s_lshl_b32 s28, s28, 4
	s_and_b32 s29, s28, 0xfffff000
	s_and_b32 s28, s28, 0xfffffc00
	s_add_i32 s28, s28, 0x8000
	s_sub_i32 s29, 0x8000, s29
	s_mul_i32 s25, s33, 0x9000
	s_add_i32 s22, s25, 0x8000
	v_lshl_add_u32 v130, v207, 4, s22
	v_lshl_add_u32 v189, v1, 4, v130
	v_lshlrev_b32_e32 v130, 4, v227
	v_add3_u32 v240, s25, v130, v206
	v_add3_u32 v187, s25, v130, v206
	ds_read_b128 v[130:133], v189 offset:32768
	ds_read_b128 v[134:137], v189 offset:32800
	ds_read_b128 v[138:141], v189 offset:32832
	ds_read_b128 v[142:145], v189 offset:32864
	ds_read_b128 v[190:193], v240 offset:32768
	ds_read_b128 v[194:197], v240 offset:33792
	ds_read_b128 v[198:201], v240 offset:34816
	ds_read_b128 v[202:205], v240 offset:35840
	ds_read_b128 v[212:215], v240 offset:36864
	ds_read_b128 v[228:231], v240 offset:37888
	ds_read_b128 v[232:235], v240 offset:38912
	ds_read_b128 v[236:239], v240 offset:39936
	s_waitcnt lgkmcnt(7)
	v_mfma_f32_32x32x16_f16 v[130:145], v[190:193], v[146:149], v[130:145]
	s_waitcnt lgkmcnt(6)
	v_mfma_f32_32x32x16_f16 v[130:145], v[194:197], v[150:153], v[130:145]
	s_waitcnt lgkmcnt(5)
	v_mfma_f32_32x32x16_f16 v[130:145], v[198:201], v[154:157], v[130:145]
	s_waitcnt lgkmcnt(4)
	v_mfma_f32_32x32x16_f16 v[130:145], v[202:205], v[158:161], v[130:145]
	s_waitcnt lgkmcnt(3)
	v_mfma_f32_32x32x16_f16 v[130:145], v[212:215], v[162:165], v[130:145]
	s_waitcnt lgkmcnt(2)
	v_mfma_f32_32x32x16_f16 v[130:145], v[228:231], v[166:169], v[130:145]
	s_waitcnt lgkmcnt(1)
	v_mfma_f32_32x32x16_f16 v[130:145], v[232:235], v[170:173], v[130:145]
	s_waitcnt lgkmcnt(0)
	v_mfma_f32_32x32x16_f16 v[130:145], v[236:239], v[174:177], v[130:145]
	s_nop 7
	s_nop 4
	v_cvt_pk_f16_f32 v246, v130, v131
	v_cvt_pk_f16_f32 v247, v132, v133
	v_cvt_pk_f16_f32 v248, v134, v135
	v_cvt_pk_f16_f32 v249, v136, v137
	v_cvt_pk_f16_f32 v250, v138, v139
	v_cvt_pk_f16_f32 v251, v140, v141
	v_cvt_pk_f16_f32 v252, v142, v143
	v_cvt_pk_f16_f32 v253, v144, v145
	s_branch .LBB1_10
.LBB1_9:
	s_or_b64 exec, exec, s[14:15]
	s_add_i32 s14, s33, 1
	s_cmp_lg_u32 s33, 2
	s_cselect_b32 s33, s14, 0
	s_add_i32 s18, s18, 1
	s_add_i32 s17, s17, 64
	s_waitcnt vmcnt(0)
	s_add_u32 s12, s12, 0x9000
	s_addc_u32 s16, s16, 0
	s_cmpk_eq_i32 s17, 0xc00
	s_waitcnt lgkmcnt(0)
	s_barrier
	s_cbranch_scc1 .LBB1_19

.LBB1_12:
	s_andn2_saveexec_b64 s[14:15], s[14:15]
	s_cbranch_execz .LBB1_17
	s_mul_i32 s25, s33, 0x9000
	s_mov_b32 s21, s25
	s_add_i32 s21, s21, 0
	s_add_i32 s22, s21, 0x8000
	s_and_b32 s19, s18, 7
	v_lshl_add_u32 v130, v207, 4, s22
	s_cmp_lg_u32 s19, 0
	v_lshl_add_u32 v189, v1, 4, v130
	s_cbranch_scc1 .LBB1_15
	ds_read_b128 v[66:69], v189 offset:33280
	ds_read_b128 v[70:73], v189 offset:33312
	ds_read_b128 v[74:77], v189 offset:33344
	ds_read_b128 v[78:81], v189 offset:33376
	ds_read_b128 v[82:85], v189 offset:33408
	ds_read_b128 v[86:89], v189 offset:33440
	ds_read_b128 v[90:93], v189 offset:33472
	ds_read_b128 v[94:97], v189 offset:33504
	ds_read_b128 v[98:101], v189 offset:33536
	ds_read_b128 v[102:105], v189 offset:33568
	ds_read_b128 v[106:109], v189 offset:33600
	ds_read_b128 v[110:113], v189 offset:33632
	ds_read_b128 v[114:117], v189 offset:33664
	ds_read_b128 v[118:121], v189 offset:33696
	ds_read_b128 v[122:125], v189 offset:33728
	ds_read_b128 v[126:129], v189 offset:33760
	s_waitcnt lgkmcnt(12)
	v_mfma_f32_32x32x16_f16 v[66:81], v[178:181], v[146:149], v[66:81]
	s_waitcnt lgkmcnt(8)
	v_mfma_f32_32x32x16_f16 v[82:97], v[178:181], v[154:157], v[82:97]
	s_waitcnt lgkmcnt(4)
	v_mfma_f32_32x32x16_f16 v[98:113], v[178:181], v[162:165], v[98:113]
	s_waitcnt lgkmcnt(0)
	v_mfma_f32_32x32x16_f16 v[114:129], v[178:181], v[170:173], v[114:129]
	v_mfma_f32_32x32x16_f16 v[66:81], v[182:185], v[150:153], v[66:81]
	v_mfma_f32_32x32x16_f16 v[82:97], v[182:185], v[158:161], v[82:97]
	v_mfma_f32_32x32x16_f16 v[98:113], v[182:185], v[166:169], v[98:113]
	v_mfma_f32_32x32x16_f16 v[114:129], v[182:185], v[174:177], v[114:129]
.LBB1_15:
	s_add_i32 s26, s33, 1
	s_cmp_lg_u32 s33, 2
	s_cselect_b32 s26, s26, 0
	s_mul_i32 s26, s26, 0x9000
	s_sub_i32 s27, s26, s25
	v_add_u32_e32 v241, s27, v189
	v_lshlrev_b32_e32 v130, 4, v227
	v_add3_u32 v240, s26, v130, v206
	ds_read_b128 v[130:133], v241 offset:32768
	ds_read_b128 v[134:137], v241 offset:32800
	ds_read_b128 v[138:141], v241 offset:32832
	ds_read_b128 v[142:145], v241 offset:32864
	ds_read_b128 v[190:193], v240 offset:32768
	ds_read_b128 v[194:197], v240 offset:33792
	ds_read_b128 v[198:201], v240 offset:34816
	ds_read_b128 v[202:205], v240 offset:35840
	ds_read_b128 v[212:215], v240 offset:36864
	ds_read_b128 v[228:231], v240 offset:37888
	ds_read_b128 v[232:235], v240 offset:38912
	ds_read_b128 v[236:239], v240 offset:39936
	v_and_b32_e32 v242, 0x7fff7fff, v246
	v_and_b32_e32 v243, 0x7fff7fff, v247
	v_and_b32_e32 v244, 0x7fff7fff, v248
	v_and_b32_e32 v245, 0x7fff7fff, v249
	v_pk_min_f16 v242, v242, v186
	v_pk_min_f16 v243, v243, v186
	v_pk_min_f16 v244, v244, v186
	v_pk_min_f16 v245, v245, v186
	s_waitcnt lgkmcnt(7)
	v_mfma_f32_32x32x16_f16 v[130:145], v[190:193], v[146:149], v[130:145]
	ds_read_b128 v[190:193], v187 offset:40960
	v_pk_max_f16 v246, v246, 0
	v_pk_max_f16 v247, v247, 0
	v_pk_max_f16 v248, v248, 0
	v_pk_max_f16 v249, v249, 0
	v_pk_fma_f16 v242, v242, s53, -1.0 op_sel_hi:[1,0,0]
	v_pk_fma_f16 v243, v243, s53, -1.0 op_sel_hi:[1,0,0]
	s_waitcnt lgkmcnt(7)
	v_mfma_f32_32x32x16_f16 v[130:145], v[194:197], v[150:153], v[130:145]
	ds_read_b128 v[194:197], v187 offset:41984
	v_pk_fma_f16 v244, v244, s53, -1.0 op_sel_hi:[1,0,0]
	v_pk_fma_f16 v245, v245, s53, -1.0 op_sel_hi:[1,0,0]
	v_pk_fma_f16 v254, v242, s54, v188 op_sel_hi:[1,0,0]
	v_pk_fma_f16 v255, v243, s54, v188 op_sel_hi:[1,0,0]
	v_pk_fma_f16 v240, v244, s54, v188 op_sel_hi:[1,0,0]
	v_pk_fma_f16 v241, v245, s54, v188 op_sel_hi:[1,0,0]
	s_waitcnt lgkmcnt(7)
	v_mfma_f32_32x32x16_f16 v[130:145], v[198:201], v[154:157], v[130:145]
	ds_read_b128 v[198:201], v187 offset:43008
	v_pk_fma_f16 v254, v242, v254, s55 op_sel_hi:[1,1,0]
	v_pk_fma_f16 v255, v243, v255, s55 op_sel_hi:[1,1,0]
	v_pk_fma_f16 v240, v244, v240, s55 op_sel_hi:[1,1,0]
	v_pk_fma_f16 v241, v245, v241, s55 op_sel_hi:[1,1,0]
	v_pk_fma_f16 v254, v242, v254, s56 op_sel_hi:[1,1,0]
	v_pk_fma_f16 v255, v243, v255, s56 op_sel_hi:[1,1,0]
	s_waitcnt lgkmcnt(7)
	v_mfma_f32_32x32x16_f16 v[130:145], v[202:205], v[158:161], v[130:145]
	ds_read_b128 v[202:205], v187 offset:44032
	s_add_i32 s23, s20, s28
	s_add_u32 s20, s12, 0x12000
	s_addc_u32 s21, s16, 0
	s_add_i32 m0, s23, 0x0
	s_nop 0
	global_load_lds_dwordx4 v226, s[20:21]
	v_pk_fma_f16 v240, v244, v240, s56 op_sel_hi:[1,1,0]
	v_pk_fma_f16 v241, v245, v241, s56 op_sel_hi:[1,1,0]
	v_pk_fma_f16 v254, v242, v254, s57 op_sel_hi:[1,1,0]
	v_pk_fma_f16 v255, v243, v255, s57 op_sel_hi:[1,1,0]
	v_pk_fma_f16 v240, v244, v240, s57 op_sel_hi:[1,1,0]
	v_pk_fma_f16 v241, v245, v241, s57 op_sel_hi:[1,1,0]
	s_waitcnt lgkmcnt(7)
	v_mfma_f32_32x32x16_f16 v[130:145], v[212:215], v[162:165], v[130:145]
	ds_read_b128 v[212:215], v187 offset:45056
	s_add_u32 s20, s12, 0x14000
	s_addc_u32 s21, s16, 0
	s_add_i32 m0, s23, 0x2000
	s_nop 0
	global_load_lds_dwordx4 v226, s[20:21]
	v_pk_fma_f16 v254, v242, v254, s58 op_sel_hi:[1,1,0]
	v_pk_fma_f16 v255, v243, v255, s58 op_sel_hi:[1,1,0]
	v_pk_fma_f16 v240, v244, v240, s58 op_sel_hi:[1,1,0]
	v_pk_fma_f16 v241, v245, v241, s58 op_sel_hi:[1,1,0]
	s_waitcnt lgkmcnt(7)
	v_mfma_f32_32x32x16_f16 v[130:145], v[228:231], v[166:169], v[130:145]
	ds_read_b128 v[228:231], v187 offset:46080
	s_add_u32 s20, s12, 0x16000
	s_addc_u32 s21, s16, 0
	s_add_i32 m0, s23, 0x4000
	s_nop 0
	global_load_lds_dwordx4 v226, s[20:21]
	v_pk_fma_f16 v254, v242, v254, s59 op_sel_hi:[1,1,0]
	v_pk_fma_f16 v255, v243, v255, s59 op_sel_hi:[1,1,0]
	v_pk_fma_f16 v240, v244, v240, s59 op_sel_hi:[1,1,0]
	v_pk_fma_f16 v241, v245, v241, s59 op_sel_hi:[1,1,0]
	s_waitcnt lgkmcnt(7)
	v_mfma_f32_32x32x16_f16 v[130:145], v[232:235], v[170:173], v[130:145]
	ds_read_b128 v[232:235], v187 offset:47104
	s_add_u32 s20, s12, 0x18000
	s_addc_u32 s21, s16, 0
	s_add_i32 m0, s23, 0x6000
	s_nop 0
	global_load_lds_dwordx4 v226, s[20:21]
	v_pk_fma_f16 v242, v242, v254, s60 op_sel_hi:[1,1,0]
	v_pk_fma_f16 v243, v243, v255, s60 op_sel_hi:[1,1,0]
	v_pk_fma_f16 v244, v244, v240, s60 op_sel_hi:[1,1,0]
	v_pk_fma_f16 v245, v245, v241, s60 op_sel_hi:[1,1,0]
	s_waitcnt lgkmcnt(7)
	v_mfma_f32_32x32x16_f16 v[130:145], v[236:239], v[174:177], v[130:145]
	ds_read_b128 v[236:239], v187 offset:48128
	s_add_u32 s20, s12, 0x1a000
	s_addc_u32 s21, s16, 0
	s_add_i32 m0, s23, s29
	s_nop 0
	global_load_lds_dwordx4 v224, s[20:21]
	v_pk_add_f16 v246, v246, v242
	v_pk_add_f16 v247, v247, v243
	v_pk_add_f16 v248, v248, v244
	v_pk_add_f16 v249, v249, v245
	v_lshlrev_b32_e32 v187, 4, v227
	v_add3_u32 v187, s26, v187, v206
	v_and_b32_e32 v242, 0x7fff7fff, v250
	v_and_b32_e32 v243, 0x7fff7fff, v251
	v_and_b32_e32 v244, 0x7fff7fff, v252
	v_and_b32_e32 v245, 0x7fff7fff, v253
	v_pk_min_f16 v242, v242, v186
	v_pk_min_f16 v243, v243, v186
	v_pk_min_f16 v244, v244, v186
	v_pk_min_f16 v245, v245, v186
	s_waitcnt lgkmcnt(7)
	v_mfma_f32_32x32x16_f16 v[66:81], v[190:193], v[246:249], v[66:81]
	v_pk_max_f16 v250, v250, 0
	v_pk_max_f16 v251, v251, 0
	v_pk_max_f16 v252, v252, 0
	v_pk_max_f16 v253, v253, 0
	v_pk_fma_f16 v242, v242, s53, -1.0 op_sel_hi:[1,0,0]
	v_pk_fma_f16 v243, v243, s53, -1.0 op_sel_hi:[1,0,0]
	v_pk_fma_f16 v244, v244, s53, -1.0 op_sel_hi:[1,0,0]
	v_pk_fma_f16 v245, v245, s53, -1.0 op_sel_hi:[1,0,0]
	v_pk_fma_f16 v254, v242, s54, v188 op_sel_hi:[1,0,0]
	v_pk_fma_f16 v255, v243, s54, v188 op_sel_hi:[1,0,0]
	s_waitcnt lgkmcnt(5)
	v_mfma_f32_32x32x16_f16 v[82:97], v[198:201], v[246:249], v[82:97]
	v_pk_fma_f16 v240, v244, s54, v188 op_sel_hi:[1,0,0]
	v_pk_fma_f16 v241, v245, s54, v188 op_sel_hi:[1,0,0]
	v_pk_fma_f16 v254, v242, v254, s55 op_sel_hi:[1,1,0]
	v_pk_fma_f16 v255, v243, v255, s55 op_sel_hi:[1,1,0]
	v_pk_fma_f16 v240, v244, v240, s55 op_sel_hi:[1,1,0]
	v_pk_fma_f16 v241, v245, v241, s55 op_sel_hi:[1,1,0]
	v_pk_fma_f16 v254, v242, v254, s56 op_sel_hi:[1,1,0]
	v_pk_fma_f16 v255, v243, v255, s56 op_sel_hi:[1,1,0]
	v_pk_fma_f16 v240, v244, v240, s56 op_sel_hi:[1,1,0]
	v_pk_fma_f16 v241, v245, v241, s56 op_sel_hi:[1,1,0]
	s_waitcnt lgkmcnt(3)
	v_mfma_f32_32x32x16_f16 v[98:113], v[212:215], v[246:249], v[98:113]
	v_pk_fma_f16 v254, v242, v254, s57 op_sel_hi:[1,1,0]
	v_pk_fma_f16 v255, v243, v255, s57 op_sel_hi:[1,1,0]
	v_pk_fma_f16 v240, v244, v240, s57 op_sel_hi:[1,1,0]
	v_pk_fma_f16 v241, v245, v241, s57 op_sel_hi:[1,1,0]
	v_pk_fma_f16 v254, v242, v254, s58 op_sel_hi:[1,1,0]
	v_pk_fma_f16 v255, v243, v255, s58 op_sel_hi:[1,1,0]
	v_pk_fma_f16 v240, v244, v240, s58 op_sel_hi:[1,1,0]
	v_pk_fma_f16 v241, v245, v241, s58 op_sel_hi:[1,1,0]
	v_pk_fma_f16 v254, v242, v254, s59 op_sel_hi:[1,1,0]
	v_pk_fma_f16 v255, v243, v255, s59 op_sel_hi:[1,1,0]
	s_waitcnt lgkmcnt(1)
	v_mfma_f32_32x32x16_f16 v[114:129], v[232:235], v[246:249], v[114:129]
	v_pk_fma_f16 v240, v244, v240, s59 op_sel_hi:[1,1,0]
	v_pk_fma_f16 v241, v245, v241, s59 op_sel_hi:[1,1,0]
	v_pk_fma_f16 v242, v242, v254, s60 op_sel_hi:[1,1,0]
	v_pk_fma_f16 v243, v243, v255, s60 op_sel_hi:[1,1,0]
	v_pk_fma_f16 v244, v244, v240, s60 op_sel_hi:[1,1,0]
	v_pk_fma_f16 v245, v245, v241, s60 op_sel_hi:[1,1,0]
	v_pk_add_f16 v250, v250, v242
	v_pk_add_f16 v251, v251, v243
	v_pk_add_f16 v252, v252, v244
	v_pk_add_f16 v253, v253, v245
	s_nop 1
	v_mfma_f32_32x32x16_f16 v[66:81], v[194:197], v[250:253], v[66:81]
	v_mfma_f32_32x32x16_f16 v[82:97], v[202:205], v[250:253], v[82:97]
	v_mfma_f32_32x32x16_f16 v[98:113], v[228:231], v[250:253], v[98:113]
	s_waitcnt lgkmcnt(0)
	v_mfma_f32_32x32x16_f16 v[114:129], v[236:239], v[250:253], v[114:129]
	s_nop 1
	v_cvt_pk_f16_f32 v246, v130, v131
	v_cvt_pk_f16_f32 v247, v132, v133
	v_cvt_pk_f16_f32 v248, v134, v135
	v_cvt_pk_f16_f32 v249, v136, v137
	v_cvt_pk_f16_f32 v250, v138, v139
	v_cvt_pk_f16_f32 v251, v140, v141
	v_cvt_pk_f16_f32 v252, v142, v143
	v_cvt_pk_f16_f32 v253, v144, v145
	s_cmp_lg_u32 s19, 7
	s_cbranch_scc1 .LBB1_17
	ds_read_b128 v[132:135], v189 offset:33312
	ds_read_b128 v[136:139], v189 offset:33344
	ds_read_b128 v[140:143], v189 offset:33824
	ds_read_b128 v[190:193], v189 offset:33856
	ds_read_b128 v[194:197], v189 offset:33792
	ds_read_b128 v[198:201], v189 offset:33376
	ds_read_b128 v[202:205], v189 offset:33888
	s_and_b32 s19, s17, 0xe00
	v_lshl_add_u32 v130, s19, 2, v222
	ds_read_b128 v[212:215], v189 offset:33280
	ds_read_b32 v130, v130
	v_pk_add_f32 v[144:145], v[66:67], v[68:69]
	v_pk_mul_f32 v[228:229], v[66:67], v[66:67]
	v_pk_add_f32 v[230:231], v[82:83], v[84:85]
	v_pk_mul_f32 v[232:233], v[82:83], v[82:83]
	v_pk_add_f32 v[234:235], v[98:99], v[100:101]
	v_pk_mul_f32 v[236:237], v[98:99], v[98:99]
	v_pk_add_f32 v[238:239], v[114:115], v[116:117]
	v_pk_mul_f32 v[240:241], v[114:115], v[114:115]
	v_pk_fma_f32 v[228:229], v[68:69], v[68:69], v[228:229]
	v_pk_fma_f32 v[232:233], v[84:85], v[84:85], v[232:233]
	v_pk_fma_f32 v[236:237], v[100:101], v[100:101], v[236:237]
	v_pk_fma_f32 v[240:241], v[116:117], v[116:117], v[240:241]
	v_pk_add_f32 v[144:145], v[70:71], v[144:145]
	v_pk_add_f32 v[230:231], v[86:87], v[230:231]
	v_pk_add_f32 v[234:235], v[102:103], v[234:235]
	v_pk_add_f32 v[238:239], v[118:119], v[238:239]
	v_pk_fma_f32 v[228:229], v[70:71], v[70:71], v[228:229]
	v_pk_fma_f32 v[232:233], v[86:87], v[86:87], v[232:233]
	v_pk_fma_f32 v[236:237], v[102:103], v[102:103], v[236:237]
	v_pk_fma_f32 v[240:241], v[118:119], v[118:119], v[240:241]
	v_pk_add_f32 v[144:145], v[72:73], v[144:145]
	v_pk_add_f32 v[230:231], v[88:89], v[230:231]
	v_pk_add_f32 v[234:235], v[104:105], v[234:235]
	v_pk_add_f32 v[238:239], v[120:121], v[238:239]
	v_pk_fma_f32 v[228:229], v[72:73], v[72:73], v[228:229]
	v_pk_fma_f32 v[232:233], v[88:89], v[88:89], v[232:233]
	v_pk_fma_f32 v[236:237], v[104:105], v[104:105], v[236:237]
	v_pk_fma_f32 v[240:241], v[120:121], v[120:121], v[240:241]
	v_pk_add_f32 v[144:145], v[74:75], v[144:145]
	v_pk_add_f32 v[230:231], v[90:91], v[230:231]
	v_pk_add_f32 v[234:235], v[106:107], v[234:235]
	v_pk_add_f32 v[238:239], v[122:123], v[238:239]
	v_pk_fma_f32 v[228:229], v[74:75], v[74:75], v[228:229]
	v_pk_fma_f32 v[232:233], v[90:91], v[90:91], v[232:233]
	v_pk_fma_f32 v[236:237], v[106:107], v[106:107], v[236:237]
	v_pk_fma_f32 v[240:241], v[122:123], v[122:123], v[240:241]
	v_pk_add_f32 v[144:145], v[76:77], v[144:145]
	v_pk_add_f32 v[230:231], v[92:93], v[230:231]
	v_pk_add_f32 v[234:235], v[108:109], v[234:235]
	v_pk_add_f32 v[238:239], v[124:125], v[238:239]
	v_pk_fma_f32 v[228:229], v[76:77], v[76:77], v[228:229]
	v_pk_fma_f32 v[232:233], v[92:93], v[92:93], v[232:233]
	v_pk_fma_f32 v[236:237], v[108:109], v[108:109], v[236:237]
	v_pk_fma_f32 v[240:241], v[124:125], v[124:125], v[240:241]
	v_pk_add_f32 v[144:145], v[78:79], v[144:145]
	v_pk_add_f32 v[230:231], v[94:95], v[230:231]
	v_pk_add_f32 v[234:235], v[110:111], v[234:235]
	v_pk_add_f32 v[238:239], v[126:127], v[238:239]
	v_pk_fma_f32 v[228:229], v[78:79], v[78:79], v[228:229]
	v_pk_fma_f32 v[232:233], v[94:95], v[94:95], v[232:233]
	v_pk_fma_f32 v[236:237], v[110:111], v[110:111], v[236:237]
	v_pk_fma_f32 v[240:241], v[126:127], v[126:127], v[240:241]
	v_pk_add_f32 v[144:145], v[80:81], v[144:145]
	v_pk_add_f32 v[230:231], v[96:97], v[230:231]
	v_pk_add_f32 v[234:235], v[112:113], v[234:235]
	v_pk_add_f32 v[238:239], v[128:129], v[238:239]
	v_pk_fma_f32 v[228:229], v[80:81], v[80:81], v[228:229]
	v_pk_fma_f32 v[232:233], v[96:97], v[96:97], v[232:233]
	v_pk_fma_f32 v[236:237], v[112:113], v[112:113], v[236:237]
	v_pk_fma_f32 v[240:241], v[128:129], v[128:129], v[240:241]
	v_pk_add_f32 v[144:145], v[144:145], v[230:231]
	v_pk_add_f32 v[230:231], v[234:235], v[238:239]
	v_pk_add_f32 v[228:229], v[228:229], v[232:233]
	v_pk_add_f32 v[144:145], v[144:145], v[230:231]
	v_pk_add_f32 v[230:231], v[236:237], v[240:241]
	s_nop 0
	v_pk_add_f32 v[228:229], v[228:229], v[230:231]
	v_mov_b32_e32 v231, v144
	v_mov_b32_e32 v230, v228
	v_mov_b32_e32 v144, v229
	v_pk_add_f32 v[144:145], v[230:231], v[144:145]
	ds_bpermute_b32 v229, v225, v145
	ds_bpermute_b32 v228, v225, v144
	s_waitcnt lgkmcnt(0)
	v_pk_add_f32 v[144:145], v[144:145], v[228:229]
	s_nop 0
	v_pk_mul_f32 v[144:145], v[144:145], s[48:49] op_sel_hi:[1,0]
	s_nop 0
	v_fma_f32 v131, -v145, v145, v144
	v_add_f32_e32 v131, 0x3727c5ac, v131
	v_mul_f32_e32 v144, 0x4b800000, v131
	v_cmp_gt_f32_e32 vcc, s61, v131
	s_nop 1
	v_cndmask_b32_e32 v131, v131, v144, vcc
	v_rsq_f32_e32 v131, v131
	s_nop 0
	v_mul_f32_e32 v144, 0x45800000, v131
	v_cndmask_b32_e32 v144, v131, v144, vcc
	v_mul_f32_e64 v228, v144, -v145
	v_pk_fma_f32 v[230:231], v[80:81], v[144:145], v[228:229] op_sel_hi:[1,0,0]
	v_pk_fma_f32 v[232:233], v[78:79], v[144:145], v[228:229] op_sel_hi:[1,0,0]
	v_pk_fma_f32 v[234:235], v[76:77], v[144:145], v[228:229] op_sel_hi:[1,0,0]
	v_pk_fma_f32 v[236:237], v[74:75], v[144:145], v[228:229] op_sel_hi:[1,0,0]
	v_pk_fma_f32 v[238:239], v[72:73], v[144:145], v[228:229] op_sel_hi:[1,0,0]
	v_pk_fma_f32 v[240:241], v[70:71], v[144:145], v[228:229] op_sel_hi:[1,0,0]
	v_pk_fma_f32 v[242:243], v[68:69], v[144:145], v[228:229] op_sel_hi:[1,0,0]
	v_pk_fma_f32 v[244:245], v[66:67], v[144:145], v[228:229] op_sel_hi:[1,0,0]
	v_pk_fma_f32 v[196:197], v[242:243], v[214:215], v[196:197]
	v_pk_fma_f32 v[194:195], v[244:245], v[212:213], v[194:195]
	v_pk_fma_f32 v[132:133], v[240:241], v[132:133], v[140:141]
	v_pk_fma_f32 v[134:135], v[238:239], v[134:135], v[142:143]
	v_pk_fma_f32 v[136:137], v[236:237], v[136:137], v[190:191]
	v_pk_fma_f32 v[138:139], v[234:235], v[138:139], v[192:193]
	v_pk_fma_f32 v[140:141], v[232:233], v[198:199], v[202:203]
	v_pk_fma_f32 v[142:143], v[230:231], v[200:201], v[204:205]
	v_pk_fma_f32 v[14:15], v[130:131], v[140:141], v[14:15] op_sel_hi:[0,1,1]
	v_pk_fma_f32 v[16:17], v[130:131], v[142:143], v[16:17] op_sel_hi:[0,1,1]
	v_pk_fma_f32 v[12:13], v[130:131], v[138:139], v[12:13] op_sel_hi:[0,1,1]
	v_pk_fma_f32 v[10:11], v[130:131], v[136:137], v[10:11] op_sel_hi:[0,1,1]
	v_pk_fma_f32 v[8:9], v[130:131], v[134:135], v[8:9] op_sel_hi:[0,1,1]
	v_pk_fma_f32 v[6:7], v[130:131], v[132:133], v[6:7] op_sel_hi:[0,1,1]
	v_pk_fma_f32 v[4:5], v[130:131], v[196:197], v[4:5] op_sel_hi:[0,1,1]
	v_pk_fma_f32 v[2:3], v[130:131], v[194:195], v[2:3] op_sel_hi:[0,1,1]
	ds_read_b128 v[132:135], v189 offset:33408
	ds_read_b128 v[136:139], v189 offset:33440
	ds_read_b128 v[140:143], v189 offset:33920
	ds_read_b128 v[190:193], v189 offset:33952
	ds_read_b128 v[194:197], v189 offset:33472
	ds_read_b128 v[198:201], v189 offset:33504
	ds_read_b128 v[202:205], v189 offset:33984
	ds_read_b128 v[212:215], v189 offset:34016
	v_pk_fma_f32 v[230:231], v[96:97], v[144:145], v[228:229] op_sel_hi:[1,0,0]
	v_pk_fma_f32 v[232:233], v[94:95], v[144:145], v[228:229] op_sel_hi:[1,0,0]
	v_pk_fma_f32 v[234:235], v[92:93], v[144:145], v[228:229] op_sel_hi:[1,0,0]
	v_pk_fma_f32 v[236:237], v[90:91], v[144:145], v[228:229] op_sel_hi:[1,0,0]
	v_pk_fma_f32 v[238:239], v[88:89], v[144:145], v[228:229] op_sel_hi:[1,0,0]
	v_pk_fma_f32 v[240:241], v[86:87], v[144:145], v[228:229] op_sel_hi:[1,0,0]
	v_pk_fma_f32 v[242:243], v[84:85], v[144:145], v[228:229] op_sel_hi:[1,0,0]
	v_pk_fma_f32 v[244:245], v[82:83], v[144:145], v[228:229] op_sel_hi:[1,0,0]
	s_waitcnt lgkmcnt(5)
	v_pk_fma_f32 v[134:135], v[242:243], v[134:135], v[142:143]
	v_pk_fma_f32 v[132:133], v[244:245], v[132:133], v[140:141]
	s_waitcnt lgkmcnt(4)
	v_pk_fma_f32 v[136:137], v[240:241], v[136:137], v[190:191]
	v_pk_fma_f32 v[138:139], v[238:239], v[138:139], v[192:193]
	s_waitcnt lgkmcnt(1)
	v_pk_fma_f32 v[140:141], v[236:237], v[194:195], v[202:203]
	v_pk_fma_f32 v[142:143], v[234:235], v[196:197], v[204:205]
	s_waitcnt lgkmcnt(0)
	v_pk_fma_f32 v[190:191], v[232:233], v[198:199], v[212:213]
	v_pk_fma_f32 v[192:193], v[230:231], v[200:201], v[214:215]
	v_pk_fma_f32 v[62:63], v[130:131], v[190:191], v[62:63] op_sel_hi:[0,1,1]
	v_pk_fma_f32 v[64:65], v[130:131], v[192:193], v[64:65] op_sel_hi:[0,1,1]
	v_pk_fma_f32 v[60:61], v[130:131], v[142:143], v[60:61] op_sel_hi:[0,1,1]
	v_pk_fma_f32 v[58:59], v[130:131], v[140:141], v[58:59] op_sel_hi:[0,1,1]
	v_pk_fma_f32 v[56:57], v[130:131], v[138:139], v[56:57] op_sel_hi:[0,1,1]
	v_pk_fma_f32 v[54:55], v[130:131], v[136:137], v[54:55] op_sel_hi:[0,1,1]
	v_pk_fma_f32 v[52:53], v[130:131], v[134:135], v[52:53] op_sel_hi:[0,1,1]
	v_pk_fma_f32 v[50:51], v[130:131], v[132:133], v[50:51] op_sel_hi:[0,1,1]
	ds_read_b128 v[132:135], v189 offset:33536
	ds_read_b128 v[136:139], v189 offset:33568
	ds_read_b128 v[140:143], v189 offset:34048
	ds_read_b128 v[190:193], v189 offset:34080
	ds_read_b128 v[194:197], v189 offset:33600
	ds_read_b128 v[198:201], v189 offset:33632
	ds_read_b128 v[202:205], v189 offset:34112
	ds_read_b128 v[212:215], v189 offset:34144
	v_pk_fma_f32 v[230:231], v[112:113], v[144:145], v[228:229] op_sel_hi:[1,0,0]
	v_pk_fma_f32 v[232:233], v[110:111], v[144:145], v[228:229] op_sel_hi:[1,0,0]
	v_pk_fma_f32 v[234:235], v[108:109], v[144:145], v[228:229] op_sel_hi:[1,0,0]
	v_pk_fma_f32 v[236:237], v[106:107], v[144:145], v[228:229] op_sel_hi:[1,0,0]
	v_pk_fma_f32 v[238:239], v[104:105], v[144:145], v[228:229] op_sel_hi:[1,0,0]
	v_pk_fma_f32 v[240:241], v[102:103], v[144:145], v[228:229] op_sel_hi:[1,0,0]
	v_pk_fma_f32 v[242:243], v[100:101], v[144:145], v[228:229] op_sel_hi:[1,0,0]
	v_pk_fma_f32 v[244:245], v[98:99], v[144:145], v[228:229] op_sel_hi:[1,0,0]
	s_waitcnt lgkmcnt(5)
	v_pk_fma_f32 v[134:135], v[242:243], v[134:135], v[142:143]
	v_pk_fma_f32 v[132:133], v[244:245], v[132:133], v[140:141]
	s_waitcnt lgkmcnt(4)
	v_pk_fma_f32 v[136:137], v[240:241], v[136:137], v[190:191]
	v_pk_fma_f32 v[138:139], v[238:239], v[138:139], v[192:193]
	s_waitcnt lgkmcnt(1)
	v_pk_fma_f32 v[140:141], v[236:237], v[194:195], v[202:203]
	v_pk_fma_f32 v[142:143], v[234:235], v[196:197], v[204:205]
	s_waitcnt lgkmcnt(0)
	v_pk_fma_f32 v[190:191], v[232:233], v[198:199], v[212:213]
	v_pk_fma_f32 v[192:193], v[230:231], v[200:201], v[214:215]
	v_pk_fma_f32 v[46:47], v[130:131], v[190:191], v[46:47] op_sel_hi:[0,1,1]
	v_pk_fma_f32 v[48:49], v[130:131], v[192:193], v[48:49] op_sel_hi:[0,1,1]
	v_pk_fma_f32 v[44:45], v[130:131], v[142:143], v[44:45] op_sel_hi:[0,1,1]
	v_pk_fma_f32 v[42:43], v[130:131], v[140:141], v[42:43] op_sel_hi:[0,1,1]
	v_pk_fma_f32 v[40:41], v[130:131], v[138:139], v[40:41] op_sel_hi:[0,1,1]
	v_pk_fma_f32 v[38:39], v[130:131], v[136:137], v[38:39] op_sel_hi:[0,1,1]
	v_pk_fma_f32 v[36:37], v[130:131], v[134:135], v[36:37] op_sel_hi:[0,1,1]
	v_pk_fma_f32 v[34:35], v[130:131], v[132:133], v[34:35] op_sel_hi:[0,1,1]
	ds_read_b128 v[132:135], v189 offset:33664
	ds_read_b128 v[136:139], v189 offset:33696
	ds_read_b128 v[140:143], v189 offset:34176
	ds_read_b128 v[190:193], v189 offset:34208
	ds_read_b128 v[194:197], v189 offset:33728
	ds_read_b128 v[198:201], v189 offset:33760
	ds_read_b128 v[202:205], v189 offset:34240
	ds_read_b128 v[212:215], v189 offset:34272
	v_pk_fma_f32 v[230:231], v[128:129], v[144:145], v[228:229] op_sel_hi:[1,0,0]
	v_pk_fma_f32 v[232:233], v[126:127], v[144:145], v[228:229] op_sel_hi:[1,0,0]
	v_pk_fma_f32 v[234:235], v[124:125], v[144:145], v[228:229] op_sel_hi:[1,0,0]
	v_pk_fma_f32 v[236:237], v[122:123], v[144:145], v[228:229] op_sel_hi:[1,0,0]
	v_pk_fma_f32 v[238:239], v[120:121], v[144:145], v[228:229] op_sel_hi:[1,0,0]
	v_pk_fma_f32 v[240:241], v[118:119], v[144:145], v[228:229] op_sel_hi:[1,0,0]
	v_pk_fma_f32 v[242:243], v[116:117], v[144:145], v[228:229] op_sel_hi:[1,0,0]
	v_pk_fma_f32 v[144:145], v[114:115], v[144:145], v[228:229] op_sel_hi:[1,0,0]
	s_waitcnt lgkmcnt(5)
	v_pk_fma_f32 v[134:135], v[242:243], v[134:135], v[142:143]
	v_pk_fma_f32 v[132:133], v[144:145], v[132:133], v[140:141]
	s_waitcnt lgkmcnt(4)
	v_pk_fma_f32 v[136:137], v[240:241], v[136:137], v[190:191]
	v_pk_fma_f32 v[138:139], v[238:239], v[138:139], v[192:193]
	s_waitcnt lgkmcnt(1)
	v_pk_fma_f32 v[140:141], v[236:237], v[194:195], v[202:203]
	v_pk_fma_f32 v[142:143], v[234:235], v[196:197], v[204:205]
	s_waitcnt lgkmcnt(0)
	v_pk_fma_f32 v[144:145], v[232:233], v[198:199], v[212:213]
	v_pk_fma_f32 v[190:191], v[230:231], v[200:201], v[214:215]
	v_pk_fma_f32 v[30:31], v[130:131], v[144:145], v[30:31] op_sel_hi:[0,1,1]
	v_pk_fma_f32 v[32:33], v[130:131], v[190:191], v[32:33] op_sel_hi:[0,1,1]
	v_pk_fma_f32 v[28:29], v[130:131], v[142:143], v[28:29] op_sel_hi:[0,1,1]
	v_pk_fma_f32 v[26:27], v[130:131], v[140:141], v[26:27] op_sel_hi:[0,1,1]
	v_pk_fma_f32 v[24:25], v[130:131], v[138:139], v[24:25] op_sel_hi:[0,1,1]
	v_pk_fma_f32 v[22:23], v[130:131], v[136:137], v[22:23] op_sel_hi:[0,1,1]
	v_pk_fma_f32 v[20:21], v[130:131], v[134:135], v[20:21] op_sel_hi:[0,1,1]
	v_pk_fma_f32 v[18:19], v[130:131], v[132:133], v[18:19] op_sel_hi:[0,1,1]

	.amdhsa_kernel _Z10ple_kernelPKfPKDv8_DF16_PKcS0_S0_S0_S0_S0_S0_Pf
		.amdhsa_group_segment_fixed_size 0
		.amdhsa_private_segment_fixed_size 0
		.amdhsa_kernarg_size 80
		.amdhsa_user_sgpr_count 2
		.amdhsa_user_sgpr_dispatch_ptr 0
		.amdhsa_user_sgpr_queue_ptr 0
		.amdhsa_user_sgpr_kernarg_segment_ptr 1
		.amdhsa_user_sgpr_dispatch_id 0
		.amdhsa_user_sgpr_kernarg_preload_length 0
		.amdhsa_user_sgpr_kernarg_preload_offset 0
		.amdhsa_user_sgpr_private_segment_size 0
		.amdhsa_uses_dynamic_stack 0
		.amdhsa_enable_private_segment 0
		.amdhsa_system_sgpr_workgroup_id_x 1
		.amdhsa_system_sgpr_workgroup_id_y 0
		.amdhsa_system_sgpr_workgroup_id_z 0
		.amdhsa_system_sgpr_workgroup_info 0
		.amdhsa_system_vgpr_workitem_id 0
		.amdhsa_next_free_vgpr 256
		.amdhsa_next_free_sgpr 63
		.amdhsa_accum_offset 256
		.amdhsa_reserve_vcc 1
		.amdhsa_float_round_mode_32 0
		.amdhsa_float_round_mode_16_64 0
		.amdhsa_float_denorm_mode_32 3
		.amdhsa_float_denorm_mode_16_64 3
		.amdhsa_dx10_clamp 1
		.amdhsa_ieee_mode 1
		.amdhsa_fp16_overflow 0
		.amdhsa_tg_split 0
		.amdhsa_exception_fp_ieee_invalid_op 0
		.amdhsa_exception_fp_denorm_src 0
		.amdhsa_exception_fp_ieee_div_zero 0
		.amdhsa_exception_fp_ieee_overflow 0
		.amdhsa_exception_fp_ieee_underflow 0
		.amdhsa_exception_fp_ieee_inexact 0
		.amdhsa_exception_int_div_zero 0
	.end_amdhsa_kernel

amdhsa.kernels:
  - .agpr_count:     0
    .args:
      - .actual_access:  read_only
        .address_space:  global
        .offset:         0
        .size:           8
        .value_kind:     global_buffer
      - .actual_access:  read_only
        .address_space:  global
        .offset:         8
        .size:           8
        .value_kind:     global_buffer
      - .actual_access:  read_only
        .address_space:  global
        .offset:         16
        .size:           8
        .value_kind:     global_buffer
      - .actual_access:  read_only
        .address_space:  global
        .offset:         24
        .size:           8
        .value_kind:     global_buffer
      - .actual_access:  read_only
        .address_space:  global
        .offset:         32
        .size:           8
        .value_kind:     global_buffer
      - .actual_access:  read_only
        .address_space:  global
        .offset:         40
        .size:           8
        .value_kind:     global_buffer
      - .actual_access:  read_only
        .address_space:  global
        .offset:         48
        .size:           8
        .value_kind:     global_buffer
      - .actual_access:  read_only
        .address_space:  global
        .offset:         56
        .size:           8
        .value_kind:     global_buffer
      - .actual_access:  read_only
        .address_space:  global
        .offset:         64
        .size:           8
        .value_kind:     global_buffer
      - .actual_access:  read_only
        .address_space:  global
        .offset:         72
        .size:           8
        .value_kind:     global_buffer
      - .actual_access:  write_only
        .address_space:  global
        .offset:         80
        .size:           8
        .value_kind:     global_buffer
      - .actual_access:  write_only
        .address_space:  global
        .offset:         88
        .size:           8
        .value_kind:     global_buffer
    .group_segment_fixed_size: 0
    .kernarg_segment_align: 8
    .kernarg_segment_size: 96
    .language:       OpenCL C
    .language_version:
      - 2
      - 0
    .max_flat_workgroup_size: 1024
    .name:           _Z11prep_kernelPKfS0_S0_S0_S0_S0_S0_S0_S0_S0_PDv8_DF16_S2_
    .private_segment_fixed_size: 0
    .sgpr_count:     34
    .sgpr_spill_count: 0
    .symbol:         _Z11prep_kernelPKfS0_S0_S0_S0_S0_S0_S0_S0_S0_PDv8_DF16_S2_.kd
    .uniform_work_group_size: 1
    .uses_dynamic_stack: false
    .vgpr_count:     23
    .vgpr_spill_count: 0
    .wavefront_size: 64
  - .agpr_count:     0
    .args:
      - .actual_access:  read_only
        .address_space:  global
        .offset:         0
        .size:           8
        .value_kind:     global_buffer
      - .actual_access:  read_only
        .address_space:  global
        .offset:         8
        .size:           8
        .value_kind:     global_buffer
      - .address_space:  global
        .offset:         16
        .size:           8
        .value_kind:     global_buffer
      - .actual_access:  read_only
        .address_space:  global
        .offset:         24
        .size:           8
        .value_kind:     global_buffer
      - .actual_access:  read_only
        .address_space:  global
        .offset:         32
        .size:           8
        .value_kind:     global_buffer
      - .actual_access:  read_only
        .address_space:  global
        .offset:         40
        .size:           8
        .value_kind:     global_buffer
      - .actual_access:  read_only
        .address_space:  global
        .offset:         48
        .size:           8
        .value_kind:     global_buffer
      - .actual_access:  read_only
        .address_space:  global
        .offset:         56
        .size:           8
        .value_kind:     global_buffer
      - .actual_access:  read_only
        .address_space:  global
        .offset:         64
        .size:           8
        .value_kind:     global_buffer
      - .actual_access:  write_only
        .address_space:  global
        .offset:         72
        .size:           8
        .value_kind:     global_buffer
    .group_segment_fixed_size: 0
    .kernarg_segment_align: 8
    .kernarg_segment_size: 80
    .language:       OpenCL C
    .language_version:
      - 2
      - 0
    .max_flat_workgroup_size: 512
    .name:           _Z10ple_kernelPKfPKDv8_DF16_PKcS0_S0_S0_S0_S0_S0_Pf
    .private_segment_fixed_size: 0
    .sgpr_count:     69
    .sgpr_spill_count: 0
    .symbol:         _Z10ple_kernelPKfPKDv8_DF16_PKcS0_S0_S0_S0_S0_S0_Pf.kd
    .uniform_work_group_size: 1
    .uses_dynamic_stack: false
    .vgpr_count:     256
    .vgpr_spill_count: 0
    .wavefront_size: 64
